# speedup vs baseline: 1.0040x; 1.0040x over previous
_Z11lstm_kernelPKiPKhPKfS4_S4_Pf:
	s_load_dwordx4 s[12:15], s[0:1], 0x0
	v_readfirstlane_b32 s19, v0
	v_or_b32_e32 v3, 0x400, v0
	s_movk_i32 s4, 0x500
	s_lshr_b32 s7, s19, 6
	s_lshl_b32 s18, s2, 6
	s_mulk_i32 s2, 0x1400
	v_mov_b32_e32 v2, 0x4ff
	v_cmp_gt_u32_e32 vcc, s4, v3
	s_mul_hi_i32 s3, s18, 0x50
	s_waitcnt lgkmcnt(0)
	s_add_u32 s2, s12, s2
	v_cndmask_b32_e32 v2, v2, v3, vcc
	s_addc_u32 s3, s13, s3
	v_lshlrev_b32_e32 v1, 2, v0
	v_lshlrev_b32_e32 v4, 2, v2
	s_movk_i32 s4, 0x184
	v_or_b32_e32 v28, 0x200, v0
	global_load_dword v29, v1, s[2:3]
	global_load_dword v30, v1, s[2:3] offset:2048
	global_load_dword v2, v4, s[2:3]
	v_mov_b32_e32 v4, 0x383
	v_cmp_gt_u32_e32 vcc, s4, v0
	s_add_u32 s2, s14, 0x34000
	s_addc_u32 s3, s15, 0
	v_cndmask_b32_e32 v4, v4, v28, vcc
	v_lshlrev_b32_e32 v31, 4, v0
	v_lshlrev_b32_e32 v4, 4, v4
	global_load_dwordx4 v[6:9], v31, s[2:3]
	global_load_dwordx4 v[10:13], v4, s[2:3]
	v_and_b32_e32 v4, 0x7f, v0
	v_lshlrev_b32_e32 v18, 4, v4
	v_mov_b32_e32 v19, 0
	v_lshl_add_u64 v[4:5], s[14:15], 0, v[18:19]
	s_mov_b32 s2, 0x37000
	v_add_co_u32_e64 v4, s[2:3], s2, v4
	s_nop 1
	v_addc_co_u32_e64 v5, s[2:3], 0, v5, s[2:3]
	global_load_dwordx4 v[14:17], v[4:5], off offset:2112
	s_movk_i32 s22, 0x410
	s_movk_i32 s2, 0x4ff
	v_and_b32_e32 v4, 63, v0
	v_cmp_lt_u32_e64 s[2:3], s2, v3
	s_mul_i32 s5, s7, 0x6000
	s_mul_hi_u32 s4, s7, 0x6000
	s_add_u32 s8, s14, s5
	s_addc_u32 s9, s15, s4
	v_lshlrev_b32_e32 v210, 4, v4
	v_mov_b32_e32 v211, v19
	v_lshl_add_u64 v[20:21], s[8:9], 0, v[210:211]
	s_movk_i32 s4, 0x2000
	v_add_co_u32_e64 v22, s[4:5], s4, v20
	s_nop 1
	v_addc_co_u32_e64 v23, s[4:5], 0, v21, s[4:5]
	s_movk_i32 s4, 0x3000
	s_nop 0
	v_add_co_u32_e64 v24, s[4:5], s4, v20
	global_load_dwordx4 v[90:93], v[22:23], off offset:1024
	global_load_dwordx4 v[86:89], v[22:23], off offset:2048
	v_addc_co_u32_e64 v25, s[4:5], 0, v21, s[4:5]
	s_movk_i32 s4, 0x5000
	s_nop 0
	v_add_co_u32_e64 v26, s[4:5], s4, v20
	s_nop 1
	v_addc_co_u32_e64 v27, s[4:5], 0, v21, s[4:5]
	global_load_dwordx4 v[82:85], v[22:23], off offset:3072
	global_load_dwordx4 v[46:49], v[26:27], off
	global_load_dwordx4 v[42:45], v[26:27], off offset:1024
	global_load_dwordx4 v[38:41], v[26:27], off offset:2048
	global_load_dwordx4 v[94:97], v[24:25], off offset:-4096
	global_load_dwordx4 v[34:37], v[26:27], off offset:3072
	s_movk_i32 s4, 0x1000
	v_add_co_u32_e64 v22, s[4:5], s4, v20
	global_load_dwordx4 v[126:129], v210, s[8:9]
	global_load_dwordx4 v[122:125], v210, s[8:9] offset:1024
	global_load_dwordx4 v[118:121], v210, s[8:9] offset:2048
	global_load_dwordx4 v[114:117], v210, s[8:9] offset:3072
	v_addc_co_u32_e64 v23, s[4:5], 0, v21, s[4:5]
	global_load_dwordx4 v[110:113], v[22:23], off
	global_load_dwordx4 v[106:109], v[22:23], off offset:1024
	global_load_dwordx4 v[102:105], v[22:23], off offset:2048
	global_load_dwordx4 v[98:101], v[22:23], off offset:3072
	global_load_dwordx4 v[78:81], v[24:25], off
	global_load_dwordx4 v[74:77], v[24:25], off offset:1024
	global_load_dwordx4 v[70:73], v[24:25], off offset:2048
	global_load_dwordx4 v[66:69], v[24:25], off offset:3072
	s_movk_i32 s4, 0x4000
	v_add_co_u32_e64 v20, s[4:5], s4, v20
	v_mov_b32_e32 v5, 0x4000
	s_nop 0
	v_addc_co_u32_e64 v21, s[4:5], 0, v21, s[4:5]
	global_load_dwordx4 v[62:65], v[20:21], off
	global_load_dwordx4 v[58:61], v[20:21], off offset:1024
	global_load_dwordx4 v[54:57], v[20:21], off offset:2048
	global_load_dwordx4 v[50:53], v[20:21], off offset:3072
	s_waitcnt vmcnt(26)
	ds_write_b128 v31, v[6:9] offset:16384
	v_lshl_or_b32 v5, v28, 4, v5
	v_add_u32_e32 v6, 0x9840, v31
	v_cndmask_b32_e32 v5, v6, v5, vcc
	s_waitcnt vmcnt(25)
	ds_write_b128 v5, v[10:13]
	s_waitcnt vmcnt(24)
	ds_write_b128 v18, v[14:17] offset:36928
	v_mul_u32_u24_e32 v5, 0xccd, v0
	v_lshrrev_b32_e32 v5, 16, v5
	s_mov_b32 s5, 0xffffec
	v_mul_u32_u24_e32 v6, 0xccd, v28
	s_movk_i32 s4, 0x90
	v_mad_u32_u24 v8, v5, s5, v0
	v_lshlrev_b32_e32 v5, 2, v5
	v_lshrrev_b32_e32 v6, 16, v6
	v_mul_lo_u32 v7, v29, s4
	v_lshl_or_b32 v5, v8, 8, v5
	ds_write_b32 v5, v7 offset:30784
	v_mul_lo_u32 v196, v29, s22
	v_add_u32_e32 v197, 0x24e80, v5
	ds_write_b32 v197, v196
	v_mad_u32_u24 v7, v6, s5, v28
	v_lshlrev_b32_e32 v6, 2, v6
	v_mul_lo_u32 v5, v30, s4
	v_lshl_or_b32 v6, v7, 8, v6
	ds_write_b32 v6, v5 offset:30784
	v_mul_lo_u32 v198, v30, s22
	v_add_u32_e32 v199, 0x24e80, v6
	ds_write_b32 v199, v198
	s_and_saveexec_b64 s[4:5], s[2:3]
	s_xor_b64 s[2:3], exec, s[4:5]
	v_mov_b32_e32 v3, 0x9840
	v_lshl_add_u32 v5, v0, 2, v3
	s_andn2_saveexec_b64 s[2:3], s[2:3]
	v_mul_u32_u24_e32 v5, 0xccd, v3
	s_mov_b32 s4, 0xffffec
	v_mul_u32_u24_sdwa v6, v5, s4 dst_sel:DWORD dst_unused:UNUSED_PAD src0_sel:WORD_1 src1_sel:DWORD
	v_add_lshl_u32 v3, v6, v3, 8
	v_mov_b32_e32 v6, 2
	v_lshlrev_b32_sdwa v5, v6, v5 dst_sel:DWORD dst_unused:UNUSED_PAD src0_sel:DWORD src1_sel:WORD_1
	s_movk_i32 s4, 0x7840
	v_add3_u32 v5, v5, v3, s4
	s_or_b64 exec, exec, s[2:3]
	v_lshrrev_b32_e32 v3, 5, v4
	s_movk_i32 s2, 0x90
	s_lshl_b32 s6, s7, 10
	s_mulk_i32 s7, 0xfd00
	v_and_b32_e32 v182, 31, v0
	v_mul_lo_u32 v200, v2, s22
	v_mul_lo_u32 v2, v2, s2
	s_add_i32 s7, s6, s7
	v_lshlrev_b32_e32 v229, 6, v3
	ds_write_b32 v5, v2
	v_add_u32_e32 v201, 0x1d640, v5
	ds_write_b32 v201, v200
	v_lshlrev_b32_e32 v230, 4, v3
	v_lshlrev_b32_e32 v228, 2, v182
	v_or_b32_e32 v2, s7, v229
	s_waitcnt lgkmcnt(0)
	s_barrier
	s_cmpk_lt_u32 s19, 0x100
	s_cbranch_scc1 .Llight_path
	s_setprio 1
	v_add_u32_e32 v3, 0x7800, v228
	ds_read2_b32 v[138:139], v3 offset0:16 offset1:48
	ds_read_b128 v[18:21], v2 offset:36928
	ds_read_b128 v[22:25], v2 offset:36944
	s_waitcnt lgkmcnt(2)
	v_add_u32_e32 v3, v230, v138
	ds_read_b128 v[26:29], v2 offset:36960
	ds_read_b128 v[30:33], v2 offset:36976
	ds_read_b128 v[142:145], v3 offset:16384
	ds_read_b128 v[130:133], v3 offset:16416
	ds_read_b128 v[154:157], v3 offset:16448
	ds_read_b128 v[134:137], v3 offset:16480
	ds_read_b128 v[248:251], v2 offset:37104
	ds_read_b128 v[244:247], v2 offset:37088
	ds_read_b128 v[240:243], v2 offset:37072
	ds_read_b128 v[236:239], v2 offset:37056
	s_waitcnt vmcnt(17) lgkmcnt(7)
	v_mfma_f32_32x32x16_bf16 v[18:33], v[94:97], v[142:145], v[18:33]
	s_waitcnt lgkmcnt(6)
	v_mfma_f32_32x32x16_bf16 v[18:33], v[90:93], v[130:133], v[18:33]
	s_waitcnt lgkmcnt(5)
	v_mfma_f32_32x32x16_bf16 v[18:33], v[86:89], v[154:157], v[18:33]
	s_waitcnt lgkmcnt(4)
	v_mfma_f32_32x32x16_bf16 v[18:33], v[82:85], v[134:137], v[18:33]
	s_cmpk_lt_u32 s19, 0x100
	s_cselect_b64 s[2:3], -1, 0
	ds_read_b32 v158, v228 offset:31040
	v_add_u32_e32 v159, v230, v139
	s_nop 2
	v_exp_f32_e32 v139, v20
	v_exp_f32_e32 v138, v24
	v_exp_f32_e32 v141, v28
	v_exp_f32_e32 v140, v32
	v_exp_f32_e32 v18, v18
	v_exp_f32_e32 v20, v22
	v_exp_f32_e32 v22, v26
	v_add_f32_e32 v24, 1.0, v138
	v_add_f32_e32 v26, 1.0, v141
	v_add_f32_e32 v19, 1.0, v139
	v_exp_f32_e32 v23, v30
	v_add_f32_e32 v27, 1.0, v140
	v_fmac_f32_e32 v24, v20, v24
	v_fmac_f32_e32 v26, v22, v26
	v_fmac_f32_e32 v19, v18, v19
	v_fmac_f32_e32 v27, v23, v27
	v_rcp_f32_e32 v18, v24
	v_rcp_f32_e32 v22, v27
	v_rcp_f32_e32 v19, v19
	v_rcp_f32_e32 v23, v26
	v_exp_f32_e32 v146, v21
	v_exp_f32_e32 v147, v25
	s_mov_b32 s8, 0xc038aa3b
	s_mov_b32 s4, 0x4038aa3b
	v_mov_b64_e32 v[160:161], s[8:9]
	v_exp_f32_e32 v148, v29
	v_exp_f32_e32 v149, v33
	v_pk_fma_f32 v[20:21], v[138:139], s[4:5], v[160:161] op_sel_hi:[1,0,0]
	s_nop 0
	v_pk_mul_f32 v[214:215], v[20:21], v[18:19]
	v_pk_fma_f32 v[18:19], v[140:141], s[4:5], v[160:161] op_sel_hi:[1,0,0]
	s_nop 0
	v_pk_mul_f32 v[212:213], v[18:19], v[22:23]
	v_add_u32_e32 v231, s7, v229
	ds_read_b128 v[18:21], v231 offset:36928
	ds_read_b128 v[22:25], v231 offset:36944
	ds_read_b128 v[26:29], v231 offset:36960
	ds_read_b128 v[30:33], v231 offset:36976
	s_waitcnt lgkmcnt(5)
	v_mfma_f32_32x32x16_bf16 v[2:17], v[46:49], v[142:145], v[236:251]
	ds_read_b128 v[138:141], v159 offset:16384
	v_add_f32_e32 v162, 1.0, v146
	v_exp_f32_e32 v163, v215
	v_exp_f32_e32 v164, v214
	v_exp_f32_e32 v165, v213
	v_exp_f32_e32 v166, v212
	v_add_f32_e32 v142, 1.0, v147
	v_add_f32_e32 v143, 1.0, v148
	v_add_f32_e32 v144, 1.0, v149
	v_mfma_f32_32x32x16_bf16 v[2:17], v[42:45], v[130:133], v[2:17]
	ds_read_b128 v[146:149], v159 offset:16416
	v_fmac_f32_e32 v162, v162, v163
	v_fmac_f32_e32 v142, v142, v164
	v_fmac_f32_e32 v143, v143, v165
	v_fmac_f32_e32 v144, v144, v166
	v_mfma_f32_32x32x16_bf16 v[2:17], v[38:41], v[154:157], v[2:17]
	ds_read_b128 v[150:153], v159 offset:16448
	v_rcp_f32_e32 v130, v162
	v_rcp_f32_e32 v131, v142
	v_rcp_f32_e32 v132, v143
	v_rcp_f32_e32 v133, v144
	s_waitcnt vmcnt(16)
	v_mfma_f32_32x32x16_bf16 v[2:17], v[34:37], v[134:137], v[2:17]
	ds_read_b128 v[178:181], v159 offset:16480
	v_fma_f32 v130, -v163, v130, v130
	v_fma_f32 v131, -v164, v131, v131
	v_fma_f32 v132, -v165, v132, v132
	v_fma_f32 v133, -v166, v133, v133
	v_add_u32_e32 v211, s6, v210
	v_cvt_pk_bf16_f32 v130, v130, v131
	v_cvt_pk_bf16_f32 v131, v132, v133
	ds_write_b64 v211, v[130:131]
	s_nop 3
	v_exp_f32_e32 v131, v4
	v_exp_f32_e32 v130, v8
	v_exp_f32_e32 v133, v12
	v_exp_f32_e32 v132, v16
	v_exp_f32_e32 v2, v2
	v_exp_f32_e32 v4, v6
	v_exp_f32_e32 v6, v10
	v_exp_f32_e32 v7, v14
	v_add_f32_e32 v3, 1.0, v131
	v_add_f32_e32 v8, 1.0, v130
	v_add_f32_e32 v10, 1.0, v133
	v_add_f32_e32 v11, 1.0, v132
	v_fmac_f32_e32 v3, v2, v3
	v_fmac_f32_e32 v8, v4, v8
	v_fmac_f32_e32 v10, v6, v10
	v_fmac_f32_e32 v11, v7, v11
	v_rcp_f32_e32 v3, v3
	v_rcp_f32_e32 v2, v8
	v_rcp_f32_e32 v7, v10
	v_rcp_f32_e32 v6, v11
	v_exp_f32_e32 v134, v5
	v_exp_f32_e32 v135, v9
	v_pk_fma_f32 v[4:5], v[130:131], s[4:5], v[160:161] op_sel_hi:[1,0,0]
	v_exp_f32_e32 v130, v13
	v_pk_mul_f32 v[204:205], v[4:5], v[2:3]
	v_pk_fma_f32 v[2:3], v[132:133], s[4:5], v[160:161] op_sel_hi:[1,0,0]
	v_exp_f32_e32 v131, v17
	v_pk_mul_f32 v[202:203], v[2:3], v[6:7]
	s_waitcnt lgkmcnt(4)
	v_mfma_f32_32x32x16_bf16 v[18:33], v[94:97], v[138:141], v[18:33]
	v_add_f32_e32 v132, 1.0, v134
	v_exp_f32_e32 v133, v205
	v_add_f32_e32 v134, 1.0, v135
	v_exp_f32_e32 v135, v204
	v_exp_f32_e32 v136, v203
	v_exp_f32_e32 v137, v202
	v_add_f32_e32 v130, 1.0, v130
	v_add_f32_e32 v131, 1.0, v131
	s_waitcnt lgkmcnt(3)
	v_mfma_f32_32x32x16_bf16 v[18:33], v[90:93], v[146:149], v[18:33]
	v_fmac_f32_e32 v132, v132, v133
	v_fmac_f32_e32 v134, v134, v135
	v_fmac_f32_e32 v130, v130, v136
	v_fmac_f32_e32 v131, v131, v137
	s_waitcnt lgkmcnt(2)
	v_mfma_f32_32x32x16_bf16 v[18:33], v[86:89], v[150:153], v[18:33]
	v_rcp_f32_e32 v132, v132
	v_rcp_f32_e32 v134, v134
	v_rcp_f32_e32 v130, v130
	v_rcp_f32_e32 v131, v131
	s_waitcnt lgkmcnt(1)
	v_mfma_f32_32x32x16_bf16 v[18:33], v[82:85], v[178:181], v[18:33]
	v_fma_f32 v132, -v133, v132, v132
	v_fma_f32 v133, -v135, v134, v134
	v_fma_f32 v134, -v136, v130, v130
	v_fma_f32 v131, -v137, v131, v131
	v_cvt_pk_bf16_f32 v130, v132, v133
	v_cvt_pk_bf16_f32 v131, v134, v131
	ds_write_b64 v211, v[130:131] offset:8
	s_waitcnt lgkmcnt(0)
	s_barrier
	s_load_dwordx8 s[4:11], s[0:1], 0x10
	ds_read_b32 v194, v228 offset:31168
	ds_read_b128 v[174:177], v210
	v_add_u32_e32 v183, v230, v158
	ds_read_b128 v[170:173], v210 offset:1024
	v_exp_f32_e32 v131, v20
	v_exp_f32_e32 v130, v24
	v_exp_f32_e32 v133, v28
	v_exp_f32_e32 v132, v32
	ds_read_b128 v[166:169], v210 offset:2048
	v_exp_f32_e32 v18, v18
	v_exp_f32_e32 v20, v22
	v_exp_f32_e32 v22, v26
	v_exp_f32_e32 v23, v30
	v_add_f32_e32 v19, 1.0, v131
	v_add_f32_e32 v24, 1.0, v130
	v_add_f32_e32 v26, 1.0, v133
	v_add_f32_e32 v27, 1.0, v132
	ds_read_b128 v[162:165], v210 offset:3072
	v_fmac_f32_e32 v19, v18, v19
	v_fmac_f32_e32 v24, v20, v24
	v_fmac_f32_e32 v26, v22, v26
	v_fmac_f32_e32 v27, v23, v27
	ds_read_b128 v[158:161], v210 offset:4096
	v_rcp_f32_e32 v19, v19
	v_rcp_f32_e32 v18, v24
	v_rcp_f32_e32 v23, v26
	v_rcp_f32_e32 v22, v27
	ds_read_b128 v[154:157], v210 offset:5120
	v_exp_f32_e32 v186, v21
	v_exp_f32_e32 v187, v25
	ds_read_b128 v[142:145], v210 offset:6144
	s_mov_b32 s0, 0xc038aa3b
	s_mov_b32 s12, 0x4038aa3b
	v_mov_b64_e32 v[184:185], s[0:1]
	v_pk_fma_f32 v[20:21], v[130:131], s[12:13], v[184:185] op_sel_hi:[1,0,0]
	v_exp_f32_e32 v188, v29
	v_pk_mul_f32 v[200:201], v[20:21], v[18:19]
	v_pk_fma_f32 v[18:19], v[132:133], s[12:13], v[184:185] op_sel_hi:[1,0,0]
	v_exp_f32_e32 v189, v33
	v_pk_mul_f32 v[198:199], v[18:19], v[22:23]
	ds_read_b128 v[130:133], v210 offset:7168
	ds_read_b128 v[18:21], v231 offset:36928
	ds_read_b128 v[22:25], v231 offset:36944
	ds_read_b128 v[26:29], v231 offset:36960
	ds_read_b128 v[30:33], v231 offset:36976
	v_mfma_f32_32x32x16_bf16 v[2:17], v[46:49], v[138:141], v[236:251]
	ds_read_b128 v[134:137], v183 offset:16384
	v_add_f32_e32 v186, 1.0, v186
	v_exp_f32_e32 v190, v201
	v_exp_f32_e32 v191, v200
	v_exp_f32_e32 v192, v199
	v_exp_f32_e32 v193, v198
	v_add_f32_e32 v187, 1.0, v187
	v_add_f32_e32 v188, 1.0, v188
	v_add_f32_e32 v189, 1.0, v189
	v_mfma_f32_32x32x16_bf16 v[2:17], v[42:45], v[146:149], v[2:17]
	ds_read_b128 v[138:141], v183 offset:16416
	v_fmac_f32_e32 v186, v186, v190
	v_fmac_f32_e32 v187, v187, v191
	v_fmac_f32_e32 v188, v188, v192
	v_fmac_f32_e32 v189, v189, v193
	v_mfma_f32_32x32x16_bf16 v[2:17], v[38:41], v[150:153], v[2:17]
	ds_read_b128 v[146:149], v183 offset:16448
	v_rcp_f32_e32 v186, v186
	v_rcp_f32_e32 v187, v187
	v_rcp_f32_e32 v188, v188
	v_rcp_f32_e32 v189, v189
	v_mfma_f32_32x32x16_bf16 v[2:17], v[34:37], v[178:181], v[2:17]
	ds_read_b128 v[150:153], v183 offset:16480
	v_fma_f32 v183, -v190, v186, v186
	v_fma_f32 v186, -v191, v187, v187
	v_fma_f32 v187, -v192, v188, v188
	v_fma_f32 v188, -v193, v189, v189
	s_waitcnt vmcnt(15) lgkmcnt(0)
	v_mfma_f32_32x32x16_bf16 v[18:33], v[126:129], v[174:177], v[18:33]
	v_cvt_pk_bf16_f32 v178, v183, v186
	v_cvt_pk_bf16_f32 v179, v187, v188
	ds_write_b64 v211, v[178:179] offset:8192
	s_waitcnt vmcnt(14)
	v_mfma_f32_32x32x16_bf16 v[18:33], v[122:125], v[170:173], v[18:33]
	s_nop 0
	v_exp_f32_e32 v179, v4
	v_exp_f32_e32 v178, v8
	v_exp_f32_e32 v181, v12
	v_exp_f32_e32 v180, v16
	s_waitcnt vmcnt(13)
	v_mfma_f32_32x32x16_bf16 v[18:33], v[118:121], v[166:169], v[18:33]
	v_exp_f32_e32 v2, v2
	v_exp_f32_e32 v4, v6
	v_exp_f32_e32 v7, v10
	v_exp_f32_e32 v8, v14
	v_add_f32_e32 v3, 1.0, v179
	v_add_f32_e32 v6, 1.0, v178
	v_add_f32_e32 v10, 1.0, v181
	v_add_f32_e32 v11, 1.0, v180
	s_waitcnt vmcnt(12)
	v_mfma_f32_32x32x16_bf16 v[18:33], v[114:117], v[162:165], v[18:33]
	v_fmac_f32_e32 v3, v2, v3
	v_fmac_f32_e32 v6, v4, v6
	v_fmac_f32_e32 v10, v7, v10
	v_fmac_f32_e32 v11, v8, v11
	s_waitcnt vmcnt(11)
	v_mfma_f32_32x32x16_bf16 v[18:33], v[110:113], v[158:161], v[18:33]
	v_rcp_f32_e32 v3, v3
	v_rcp_f32_e32 v2, v6
	v_rcp_f32_e32 v7, v10
	v_rcp_f32_e32 v6, v11
	s_waitcnt vmcnt(10)
	v_mfma_f32_32x32x16_bf16 v[18:33], v[106:109], v[154:157], v[18:33]
	v_exp_f32_e32 v183, v5
	v_exp_f32_e32 v186, v9
	s_waitcnt vmcnt(9)
	v_mfma_f32_32x32x16_bf16 v[18:33], v[102:105], v[142:145], v[18:33]
	v_fma_f32 v4, v178, s12, v184
	v_fma_f32 v5, v179, s12, v184
	v_exp_f32_e32 v178, v13
	v_pk_mul_f32 v[206:207], v[4:5], v[2:3]
	v_pk_fma_f32 v[2:3], v[180:181], s[12:13], v[184:185] op_sel_hi:[1,0,0]
	v_exp_f32_e32 v179, v17
	v_pk_mul_f32 v[208:209], v[2:3], v[6:7]
	s_waitcnt vmcnt(8)
	v_mfma_f32_32x32x16_bf16 v[18:33], v[98:101], v[130:133], v[18:33]
	v_mfma_f32_32x32x16_bf16 v[18:33], v[94:97], v[134:137], v[18:33]
	v_add_f32_e32 v180, 1.0, v183
	v_exp_f32_e32 v181, v207
	v_add_f32_e32 v183, 1.0, v186
	v_exp_f32_e32 v184, v206
	v_exp_f32_e32 v185, v209
	v_exp_f32_e32 v186, v208
	v_add_f32_e32 v178, 1.0, v178
	v_add_f32_e32 v179, 1.0, v179
	v_mfma_f32_32x32x16_bf16 v[18:33], v[90:93], v[138:141], v[18:33]
	v_fmac_f32_e32 v180, v180, v181
	v_fmac_f32_e32 v183, v183, v184
	v_fmac_f32_e32 v178, v178, v185
	v_fmac_f32_e32 v179, v179, v186
	v_mfma_f32_32x32x16_bf16 v[18:33], v[86:89], v[146:149], v[18:33]
	v_rcp_f32_e32 v180, v180
	v_rcp_f32_e32 v183, v183
	v_rcp_f32_e32 v178, v178
	v_rcp_f32_e32 v179, v179
	v_mfma_f32_32x32x16_bf16 v[18:33], v[82:85], v[150:153], v[18:33]
	v_fma_f32 v180, -v181, v180, v180
	v_fma_f32 v181, -v184, v183, v183
	v_fma_f32 v183, -v185, v178, v178
	v_fma_f32 v179, -v186, v179, v179
	v_cvt_pk_bf16_f32 v178, v180, v181
	v_cvt_pk_bf16_f32 v179, v183, v179
	ds_write_b64 v211, v[178:179] offset:8200
	s_waitcnt lgkmcnt(0)
	s_barrier
	v_mov_b32_e32 v178, 0x7a40
	v_lshl_add_u32 v232, v182, 2, v178
	s_mov_b32 s1, -1
	s_branch .LBB1_14

.Llight_path:
	s_waitcnt vmcnt(16)
	v_mul_u32_u24_e32 v236, 36, v228
	v_add_u32_e32 v236, v236, v230
	v_add_u32_e32 v237, s7, v229
	v_mul_u32_u24_e32 v238, 0x104, v228
	v_add_u32_e32 v238, v238, v237
	v_add_u32_e32 v238, 0xb840, v238
	ds_read_b128 v[2:5], v237 offset:36928
	ds_read_b128 v[6:9], v237 offset:36944
	ds_read_b128 v[10:13], v237 offset:36960
	ds_read_b128 v[14:17], v237 offset:36976
	ds_read_b128 v[18:21], v237 offset:37056
	ds_read_b128 v[22:25], v237 offset:37072
	ds_read_b128 v[26:29], v237 offset:37088
	ds_read_b128 v[30:33], v237 offset:37104
	ds_read_b128 v[162:165], v236 offset:16384
	ds_read_b128 v[166:169], v236 offset:16416
	ds_read_b128 v[170:173], v236 offset:16448
	ds_read_b128 v[174:177], v236 offset:16480
	s_waitcnt lgkmcnt(0)
	v_mfma_f32_32x32x16_bf16 v[2:17], v[94:97], v[162:165], v[2:17]
	v_mfma_f32_32x32x16_bf16 v[2:17], v[90:93], v[166:169], v[2:17]
	v_mfma_f32_32x32x16_bf16 v[2:17], v[86:89], v[170:173], v[2:17]
	v_mfma_f32_32x32x16_bf16 v[2:17], v[82:85], v[174:177], v[2:17]
	v_mfma_f32_32x32x16_bf16 v[18:33], v[46:49], v[162:165], v[18:33]
	ds_read_b128 v[130:133], v237 offset:36928
	ds_read_b128 v[134:137], v237 offset:36944
	ds_read_b128 v[138:141], v237 offset:36960
	v_mfma_f32_32x32x16_bf16 v[18:33], v[42:45], v[166:169], v[18:33]
	ds_read_b128 v[142:145], v237 offset:36976
	ds_read_b128 v[146:149], v237 offset:37056
	ds_read_b128 v[150:153], v237 offset:37072
	v_mfma_f32_32x32x16_bf16 v[18:33], v[38:41], v[170:173], v[18:33]
	ds_read_b128 v[154:157], v237 offset:37088
	ds_read_b128 v[158:161], v237 offset:37104
	ds_read_b128 v[178:181], v236 offset:20992
	v_mfma_f32_32x32x16_bf16 v[18:33], v[34:37], v[174:177], v[18:33]
	ds_read_b128 v[182:185], v236 offset:21024
	ds_read_b128 v[186:189], v236 offset:21056
	ds_read_b128 v[190:193], v236 offset:21088
	s_waitcnt lgkmcnt(0)
	v_mfma_f32_32x32x16_bf16 v[130:145], v[94:97], v[178:181], v[130:145]
	v_mfma_f32_32x32x16_bf16 v[130:145], v[90:93], v[182:185], v[130:145]
	v_mfma_f32_32x32x16_bf16 v[130:145], v[86:89], v[186:189], v[130:145]
	v_mfma_f32_32x32x16_bf16 v[130:145], v[82:85], v[190:193], v[130:145]
	s_nop 7
	ds_write_b128 v238, v[2:5] offset:0
	ds_write_b128 v238, v[6:9] offset:16
	ds_write_b128 v238, v[10:13] offset:32
	ds_write_b128 v238, v[14:17] offset:48
	ds_write_b128 v238, v[18:21] offset:128
	ds_write_b128 v238, v[22:25] offset:144
	ds_write_b128 v238, v[26:29] offset:160
	ds_write_b128 v238, v[30:33] offset:176
	v_mfma_f32_32x32x16_bf16 v[146:161], v[46:49], v[178:181], v[146:161]
	ds_read_b128 v[2:5], v237 offset:36928
	ds_read_b128 v[6:9], v237 offset:36944
	ds_read_b128 v[10:13], v237 offset:36960
	v_mfma_f32_32x32x16_bf16 v[146:161], v[42:45], v[182:185], v[146:161]
	ds_read_b128 v[14:17], v237 offset:36976
	ds_read_b128 v[18:21], v237 offset:37056
	ds_read_b128 v[22:25], v237 offset:37072
	v_mfma_f32_32x32x16_bf16 v[146:161], v[38:41], v[186:189], v[146:161]
	ds_read_b128 v[26:29], v237 offset:37088
	ds_read_b128 v[30:33], v237 offset:37104
	ds_read_b128 v[162:165], v236 offset:25600
	v_mfma_f32_32x32x16_bf16 v[146:161], v[34:37], v[190:193], v[146:161]
	ds_read_b128 v[166:169], v236 offset:25632
	ds_read_b128 v[170:173], v236 offset:25664
	ds_read_b128 v[174:177], v236 offset:25696
	s_waitcnt lgkmcnt(0)
	v_mfma_f32_32x32x16_bf16 v[2:17], v[94:97], v[162:165], v[2:17]
	v_mfma_f32_32x32x16_bf16 v[2:17], v[90:93], v[166:169], v[2:17]
	v_mfma_f32_32x32x16_bf16 v[2:17], v[86:89], v[170:173], v[2:17]
	v_mfma_f32_32x32x16_bf16 v[2:17], v[82:85], v[174:177], v[2:17]
	s_nop 7
	v_add_u32_e32 v239, 0x8200, v238
	ds_write_b128 v239, v[130:133] offset:0
	ds_write_b128 v239, v[134:137] offset:16
	ds_write_b128 v239, v[138:141] offset:32
	ds_write_b128 v239, v[142:145] offset:48
	ds_write_b128 v239, v[146:149] offset:128
	ds_write_b128 v239, v[150:153] offset:144
	ds_write_b128 v239, v[154:157] offset:160
	ds_write_b128 v239, v[158:161] offset:176
	v_mfma_f32_32x32x16_bf16 v[18:33], v[46:49], v[162:165], v[18:33]
	ds_read_b128 v[130:133], v237 offset:36928
	ds_read_b128 v[134:137], v237 offset:36944
	ds_read_b128 v[138:141], v237 offset:36960
	v_mfma_f32_32x32x16_bf16 v[18:33], v[42:45], v[166:169], v[18:33]
	ds_read_b128 v[142:145], v237 offset:36976
	ds_read_b128 v[146:149], v237 offset:37056
	ds_read_b128 v[150:153], v237 offset:37072
	v_mfma_f32_32x32x16_bf16 v[18:33], v[38:41], v[170:173], v[18:33]
	ds_read_b128 v[154:157], v237 offset:37088
	ds_read_b128 v[158:161], v237 offset:37104
	ds_read_b128 v[178:181], v236 offset:30208
	v_mfma_f32_32x32x16_bf16 v[18:33], v[34:37], v[174:177], v[18:33]
	ds_read_b128 v[182:185], v236 offset:30240
	ds_read_b128 v[186:189], v236 offset:30272
	ds_read_b128 v[190:193], v236 offset:30304
	s_waitcnt lgkmcnt(0)
	v_mfma_f32_32x32x16_bf16 v[130:145], v[94:97], v[178:181], v[130:145]
	v_mfma_f32_32x32x16_bf16 v[130:145], v[90:93], v[182:185], v[130:145]
	v_mfma_f32_32x32x16_bf16 v[130:145], v[86:89], v[186:189], v[130:145]
	v_mfma_f32_32x32x16_bf16 v[130:145], v[82:85], v[190:193], v[130:145]
	s_nop 7
	v_add_u32_e32 v239, 0x10400, v238
	ds_write_b128 v239, v[2:5] offset:0
	ds_write_b128 v239, v[6:9] offset:16
	ds_write_b128 v239, v[10:13] offset:32
	ds_write_b128 v239, v[14:17] offset:48
	ds_write_b128 v239, v[18:21] offset:128
	ds_write_b128 v239, v[22:25] offset:144
	ds_write_b128 v239, v[26:29] offset:160
	ds_write_b128 v239, v[30:33] offset:176
	v_mfma_f32_32x32x16_bf16 v[146:161], v[46:49], v[178:181], v[146:161]
	v_mfma_f32_32x32x16_bf16 v[146:161], v[42:45], v[182:185], v[146:161]
	v_mfma_f32_32x32x16_bf16 v[146:161], v[38:41], v[186:189], v[146:161]
	v_mfma_f32_32x32x16_bf16 v[146:161], v[34:37], v[190:193], v[146:161]
	s_nop 7
	s_nop 7
	v_cmp_gt_u32_e32 vcc, 16, v228
	s_and_saveexec_b64 s[20:21], vcc
	v_add_u32_e32 v239, 0x18600, v238
	ds_write_b128 v239, v[130:133] offset:0
	ds_write_b128 v239, v[134:137] offset:16
	ds_write_b128 v239, v[138:141] offset:32
	ds_write_b128 v239, v[142:145] offset:48
	ds_write_b128 v239, v[146:149] offset:128
	ds_write_b128 v239, v[150:153] offset:144
	ds_write_b128 v239, v[154:157] offset:160
	ds_write_b128 v239, v[158:161] offset:176
	s_or_b64 exec, exec, s[20:21]
	s_waitcnt vmcnt(0) lgkmcnt(0)
	s_nop 7
	s_nop 7
	s_waitcnt vmcnt(0)
	v_add_u32_e32 v231, s7, v229
	v_add_u32_e32 v231, 0xb840, v231
	v_add_u32_e32 v211, s6, v210
	s_mov_b32 s12, 0x4038aa3b
	v_mov_b32_e32 v235, 0xc038aa3b
	s_nop 0
	s_load_dwordx8 s[4:11], s[0:1], 0x10
	s_waitcnt lgkmcnt(0)
	v_add_u32_e32 v232, 0x24e80, v228
	ds_read_b32 v244, v232
	ds_read_b32 v245, v232 offset:128
	v_mov_b32_e32 v194, 0
	v_mov_b32_e32 v195, 0
	v_mov_b32_e32 v196, 0
	v_mov_b32_e32 v197, 0
	v_mov_b32_e32 v198, 0
	v_mov_b32_e32 v199, 0
	v_mov_b32_e32 v200, 0
	v_mov_b32_e32 v201, 0
	v_mov_b32_e32 v202, 0
	v_mov_b32_e32 v203, 0
	v_mov_b32_e32 v204, 0
	v_mov_b32_e32 v205, 0
	v_mov_b32_e32 v206, 0
	v_mov_b32_e32 v207, 0
	v_mov_b32_e32 v208, 0
	v_mov_b32_e32 v209, 0
	v_add_u32_e32 v232, 0x100, v232
	s_waitcnt lgkmcnt(0)
	v_add_u32_e32 v233, v231, v244
	v_add_u32_e32 v234, v231, v245
	ds_read_b128 v[2:5], v233 offset:0
	ds_read_b128 v[6:9], v233 offset:16
	ds_read_b128 v[10:13], v233 offset:32
	ds_read_b128 v[14:17], v233 offset:48
	ds_read_b128 v[18:21], v233 offset:128
	ds_read_b128 v[22:25], v233 offset:144
	ds_read_b128 v[26:29], v233 offset:160
	ds_read_b128 v[30:33], v233 offset:176
	ds_read_b128 v[34:37], v234 offset:0
	ds_read_b128 v[38:41], v234 offset:16
	ds_read_b128 v[42:45], v234 offset:32
	ds_read_b128 v[46:49], v234 offset:48
	s_movk_i32 s16, 18
	s_waitcnt lgkmcnt(0)
	ds_read_b128 v[82:85], v234 offset:128
	ds_read_b128 v[86:89], v234 offset:144
	ds_read_b128 v[90:93], v234 offset:160
	ds_read_b128 v[94:97], v234 offset:176
	ds_read_b32 v244, v232 offset:0
	v_exp_f32_e32 v212, v4
	v_exp_f32_e32 v213, v8
	v_exp_f32_e32 v214, v12
	v_exp_f32_e32 v215, v16
	v_exp_f32_e32 v217, v2
	v_add_f32_e32 v251, 1.0, v212
	v_exp_f32_e32 v218, v6
	v_add_f32_e32 v252, 1.0, v213
	v_exp_f32_e32 v219, v10
	v_add_f32_e32 v253, 1.0, v214
	v_exp_f32_e32 v220, v14
	v_add_f32_e32 v254, 1.0, v215
	v_fma_f32 v240, v212, s12, v235
	v_fma_f32 v241, v213, s12, v235
	v_fma_f32 v242, v214, s12, v235
	v_fma_f32 v243, v215, s12, v235
	v_fmac_f32_e32 v251, v217, v251
	v_fmac_f32_e32 v252, v218, v252
	v_fmac_f32_e32 v253, v219, v253
	v_fmac_f32_e32 v254, v220, v254
	v_rcp_f32_e32 v217, v251
	v_rcp_f32_e32 v218, v252
	v_rcp_f32_e32 v219, v253
	v_rcp_f32_e32 v220, v254
	v_exp_f32_e32 v246, v5
	v_mul_f32_e32 v194, v240, v217
	v_exp_f32_e32 v247, v9
	v_mul_f32_e32 v195, v241, v218
	v_exp_f32_e32 v248, v13
	v_mul_f32_e32 v196, v242, v219
	v_exp_f32_e32 v249, v17
	v_mul_f32_e32 v197, v243, v220
	v_exp_f32_e32 v212, v194
	v_add_f32_e32 v246, 1.0, v246
	v_exp_f32_e32 v213, v195
	v_add_f32_e32 v247, 1.0, v247
	v_exp_f32_e32 v214, v196
	v_add_f32_e32 v248, 1.0, v248
	v_exp_f32_e32 v215, v197
	v_add_f32_e32 v249, 1.0, v249
	v_fmac_f32_e32 v246, v246, v212
	v_fmac_f32_e32 v247, v247, v213
	v_fmac_f32_e32 v248, v248, v214
	v_fmac_f32_e32 v249, v249, v215
	v_rcp_f32_e32 v246, v246
	v_rcp_f32_e32 v247, v247
	v_rcp_f32_e32 v248, v248
	v_rcp_f32_e32 v249, v249
	v_fma_f32 v246, -v212, v246, v246
	v_fma_f32 v247, -v213, v247, v247
	v_fma_f32 v248, -v214, v248, v248
	v_fma_f32 v249, -v215, v249, v249
	v_cvt_pk_bf16_f32 v246, v246, v247
	v_cvt_pk_bf16_f32 v247, v248, v249
	ds_write_b64 v211, v[246:247] offset:0
	s_waitcnt lgkmcnt(1)
	v_add_u32_e32 v233, v231, v244
	ds_read_b128 v[2:5], v233 offset:0
	ds_read_b128 v[6:9], v233 offset:16
	ds_read_b128 v[10:13], v233 offset:32
	ds_read_b128 v[14:17], v233 offset:48
	v_exp_f32_e32 v212, v20
	v_exp_f32_e32 v213, v24
	v_exp_f32_e32 v214, v28
	v_exp_f32_e32 v215, v32
	v_exp_f32_e32 v217, v18
	v_add_f32_e32 v251, 1.0, v212
	v_exp_f32_e32 v218, v22
	v_add_f32_e32 v252, 1.0, v213
	v_exp_f32_e32 v219, v26
	v_add_f32_e32 v253, 1.0, v214
	v_exp_f32_e32 v220, v30
	v_add_f32_e32 v254, 1.0, v215
	v_fma_f32 v240, v212, s12, v235
	v_fma_f32 v241, v213, s12, v235
	v_fma_f32 v242, v214, s12, v235
	v_fma_f32 v243, v215, s12, v235
	v_fmac_f32_e32 v251, v217, v251
	v_fmac_f32_e32 v252, v218, v252
	v_fmac_f32_e32 v253, v219, v253
	v_fmac_f32_e32 v254, v220, v254
	v_rcp_f32_e32 v217, v251
	v_rcp_f32_e32 v218, v252
	v_rcp_f32_e32 v219, v253
	v_rcp_f32_e32 v220, v254
	v_exp_f32_e32 v246, v21
	v_mul_f32_e32 v198, v240, v217
	v_exp_f32_e32 v247, v25
	v_mul_f32_e32 v199, v241, v218
	v_exp_f32_e32 v248, v29
	v_mul_f32_e32 v200, v242, v219
	v_exp_f32_e32 v249, v33
	v_mul_f32_e32 v201, v243, v220
	v_exp_f32_e32 v212, v198
	v_add_f32_e32 v246, 1.0, v246
	v_exp_f32_e32 v213, v199
	v_add_f32_e32 v247, 1.0, v247
	v_exp_f32_e32 v214, v200
	v_add_f32_e32 v248, 1.0, v248
	v_exp_f32_e32 v215, v201
	v_add_f32_e32 v249, 1.0, v249
	v_fmac_f32_e32 v246, v246, v212
	v_fmac_f32_e32 v247, v247, v213
	v_fmac_f32_e32 v248, v248, v214
	v_fmac_f32_e32 v249, v249, v215
	v_rcp_f32_e32 v246, v246
	v_rcp_f32_e32 v247, v247
	v_rcp_f32_e32 v248, v248
	v_rcp_f32_e32 v249, v249
	v_fma_f32 v246, -v212, v246, v246
	v_fma_f32 v247, -v213, v247, v247
	v_fma_f32 v248, -v214, v248, v248
	v_fma_f32 v249, -v215, v249, v249
	v_cvt_pk_bf16_f32 v246, v246, v247
	v_cvt_pk_bf16_f32 v247, v248, v249
	ds_write_b64 v211, v[246:247] offset:8
	s_waitcnt lgkmcnt(0)
	s_barrier
	ds_read_b128 v[130:133], v210 offset:0
	ds_read_b128 v[134:137], v210 offset:1024
	ds_read_b128 v[18:21], v233 offset:128
	ds_read_b128 v[22:25], v233 offset:144
	ds_read_b128 v[26:29], v233 offset:160
	ds_read_b128 v[30:33], v233 offset:176
	ds_read_b32 v245, v232 offset:128
	v_exp_f32_e32 v212, v36
	v_exp_f32_e32 v213, v40
	v_exp_f32_e32 v214, v44
	v_exp_f32_e32 v215, v48
	ds_read_b128 v[138:141], v210 offset:2048
	ds_read_b128 v[142:145], v210 offset:3072
	v_exp_f32_e32 v217, v34
	v_add_f32_e32 v251, 1.0, v212
	v_exp_f32_e32 v218, v38
	v_add_f32_e32 v252, 1.0, v213
	v_exp_f32_e32 v219, v42
	v_add_f32_e32 v253, 1.0, v214
	v_exp_f32_e32 v220, v46
	v_add_f32_e32 v254, 1.0, v215
	v_fma_f32 v240, v212, s12, v235
	v_fma_f32 v241, v213, s12, v235
	v_fma_f32 v242, v214, s12, v235
	v_fma_f32 v243, v215, s12, v235
	ds_read_b128 v[146:149], v210 offset:4096
	ds_read_b128 v[150:153], v210 offset:5120
	v_fmac_f32_e32 v251, v217, v251
	v_fmac_f32_e32 v252, v218, v252
	v_fmac_f32_e32 v253, v219, v253
	v_fmac_f32_e32 v254, v220, v254
	ds_read_b128 v[154:157], v210 offset:6144
	ds_read_b128 v[158:161], v210 offset:7168
	v_rcp_f32_e32 v217, v251
	v_rcp_f32_e32 v218, v252
	v_rcp_f32_e32 v219, v253
	v_rcp_f32_e32 v220, v254
	v_exp_f32_e32 v246, v37
	v_mul_f32_e32 v202, v240, v217
	v_exp_f32_e32 v247, v41
	v_mul_f32_e32 v203, v241, v218
	v_exp_f32_e32 v248, v45
	v_mul_f32_e32 v204, v242, v219
	v_exp_f32_e32 v249, v49
	v_mul_f32_e32 v205, v243, v220
	v_exp_f32_e32 v212, v202
	v_add_f32_e32 v246, 1.0, v246
	v_exp_f32_e32 v213, v203
	v_add_f32_e32 v247, 1.0, v247
	v_exp_f32_e32 v214, v204
	v_add_f32_e32 v248, 1.0, v248
	v_exp_f32_e32 v215, v205
	v_add_f32_e32 v249, 1.0, v249
	v_fmac_f32_e32 v246, v246, v212
	v_fmac_f32_e32 v247, v247, v213
	v_fmac_f32_e32 v248, v248, v214
	v_fmac_f32_e32 v249, v249, v215
	v_rcp_f32_e32 v246, v246
	v_rcp_f32_e32 v247, v247
	v_rcp_f32_e32 v248, v248
	v_rcp_f32_e32 v249, v249
	v_fma_f32 v246, -v212, v246, v246
	v_fma_f32 v247, -v213, v247, v247
	v_fma_f32 v248, -v214, v248, v248
	v_fma_f32 v249, -v215, v249, v249
	v_cvt_pk_bf16_f32 v246, v246, v247
	v_cvt_pk_bf16_f32 v247, v248, v249
	ds_write_b64 v211, v[246:247] offset:8192
	s_waitcnt lgkmcnt(1)
	v_mfma_f32_32x32x16_bf16 v[2:17], v[126:129], v[130:133], v[2:17]
	v_add_u32_e32 v234, v231, v245
	ds_read_b128 v[34:37], v234 offset:0
	ds_read_b128 v[38:41], v234 offset:16
	ds_read_b128 v[42:45], v234 offset:32
	ds_read_b128 v[46:49], v234 offset:48
	v_add_u32_e32 v232, 0x100, v232
	v_exp_f32_e32 v212, v84
	v_exp_f32_e32 v213, v88
	v_exp_f32_e32 v214, v92
	v_exp_f32_e32 v215, v96
	v_mfma_f32_32x32x16_bf16 v[2:17], v[122:125], v[134:137], v[2:17]
	v_exp_f32_e32 v217, v82
	v_add_f32_e32 v251, 1.0, v212
	v_exp_f32_e32 v218, v86
	v_add_f32_e32 v252, 1.0, v213
	v_exp_f32_e32 v219, v90
	v_add_f32_e32 v253, 1.0, v214
	v_exp_f32_e32 v220, v94
	v_add_f32_e32 v254, 1.0, v215
	v_fma_f32 v240, v212, s12, v235
	v_fma_f32 v241, v213, s12, v235
	v_fma_f32 v242, v214, s12, v235
	v_fma_f32 v243, v215, s12, v235
	v_mfma_f32_32x32x16_bf16 v[2:17], v[118:121], v[138:141], v[2:17]
	v_fmac_f32_e32 v251, v217, v251
	v_fmac_f32_e32 v252, v218, v252
	v_fmac_f32_e32 v253, v219, v253
	v_fmac_f32_e32 v254, v220, v254
	v_mfma_f32_32x32x16_bf16 v[2:17], v[114:117], v[142:145], v[2:17]
	v_rcp_f32_e32 v217, v251
	v_rcp_f32_e32 v218, v252
	v_rcp_f32_e32 v219, v253
	v_rcp_f32_e32 v220, v254
	v_mfma_f32_32x32x16_bf16 v[2:17], v[110:113], v[146:149], v[2:17]
	v_exp_f32_e32 v246, v85
	v_mul_f32_e32 v206, v240, v217
	v_exp_f32_e32 v247, v89
	v_mul_f32_e32 v207, v241, v218
	v_exp_f32_e32 v248, v93
	v_mul_f32_e32 v208, v242, v219
	v_exp_f32_e32 v249, v97
	v_mul_f32_e32 v209, v243, v220
	v_mfma_f32_32x32x16_bf16 v[2:17], v[106:109], v[150:153], v[2:17]
	v_mfma_f32_32x32x16_bf16 v[2:17], v[102:105], v[154:157], v[2:17]
	v_exp_f32_e32 v212, v206
	v_add_f32_e32 v246, 1.0, v246
	v_exp_f32_e32 v213, v207
	v_add_f32_e32 v247, 1.0, v247
	v_exp_f32_e32 v214, v208
	v_add_f32_e32 v248, 1.0, v248
	v_exp_f32_e32 v215, v209
	v_add_f32_e32 v249, 1.0, v249
	v_fmac_f32_e32 v246, v246, v212
	v_fmac_f32_e32 v247, v247, v213
	v_fmac_f32_e32 v248, v248, v214
	v_fmac_f32_e32 v249, v249, v215
	v_mfma_f32_32x32x16_bf16 v[2:17], v[98:101], v[158:161], v[2:17]
	v_rcp_f32_e32 v246, v246
	v_rcp_f32_e32 v247, v247
	v_rcp_f32_e32 v248, v248
	v_rcp_f32_e32 v249, v249
	v_fma_f32 v246, -v212, v246, v246
	v_fma_f32 v247, -v213, v247, v247
	v_fma_f32 v248, -v214, v248, v248
	v_fma_f32 v249, -v215, v249, v249
	v_cvt_pk_bf16_f32 v246, v246, v247
	v_cvt_pk_bf16_f32 v247, v248, v249
	ds_write_b64 v211, v[246:247] offset:8200
	s_waitcnt lgkmcnt(0)
	s_barrier
	.p2align 6
.Llight_loop:
	v_mfma_f32_32x32x16_bf16 v[18:33], v[78:81], v[130:133], v[18:33]
	ds_read_b128 v[162:165], v210 offset:8192
	ds_read_b128 v[166:169], v210 offset:9216
	ds_read_b128 v[82:85], v234 offset:128
	ds_read_b128 v[86:89], v234 offset:144
	ds_read_b128 v[90:93], v234 offset:160
	ds_read_b128 v[94:97], v234 offset:176
	ds_read_b32 v244, v232 offset:0
	v_exp_f32_e32 v212, v4
	v_exp_f32_e32 v213, v8
	v_exp_f32_e32 v214, v12
	v_exp_f32_e32 v215, v16
	v_mfma_f32_32x32x16_bf16 v[18:33], v[74:77], v[134:137], v[18:33]
	ds_read_b128 v[170:173], v210 offset:10240
	ds_read_b128 v[174:177], v210 offset:11264
	v_exp_f32_e32 v217, v2
	v_add_f32_e32 v251, 1.0, v212
	v_exp_f32_e32 v218, v6
	v_add_f32_e32 v252, 1.0, v213
	v_exp_f32_e32 v219, v10
	v_add_f32_e32 v253, 1.0, v214
	v_exp_f32_e32 v220, v14
	v_add_f32_e32 v254, 1.0, v215
	v_fma_f32 v240, v212, s12, v235
	v_fma_f32 v241, v213, s12, v235
	v_fma_f32 v242, v214, s12, v235
	v_fma_f32 v243, v215, s12, v235
	v_mfma_f32_32x32x16_bf16 v[18:33], v[70:73], v[138:141], v[18:33]
	ds_read_b128 v[178:181], v210 offset:12288
	ds_read_b128 v[182:185], v210 offset:13312
	v_exp_f32_e32 v221, v3
	v_fmac_f32_e32 v251, v217, v251
	v_exp_f32_e32 v222, v7
	v_fmac_f32_e32 v252, v218, v252
	v_exp_f32_e32 v223, v11
	v_fmac_f32_e32 v253, v219, v253
	v_exp_f32_e32 v224, v15
	v_fmac_f32_e32 v254, v220, v254
	v_mfma_f32_32x32x16_bf16 v[18:33], v[66:69], v[142:145], v[18:33]
	ds_read_b128 v[186:189], v210 offset:14336
	ds_read_b128 v[190:193], v210 offset:15360
	v_rcp_f32_e32 v217, v251
	v_add_f32_e32 v221, 1.0, v221
	v_rcp_f32_e32 v218, v252
	v_add_f32_e32 v222, 1.0, v222
	v_rcp_f32_e32 v219, v253
	v_add_f32_e32 v223, 1.0, v223
	v_rcp_f32_e32 v220, v254
	v_add_f32_e32 v224, 1.0, v224
	v_mfma_f32_32x32x16_bf16 v[18:33], v[62:65], v[146:149], v[18:33]
	v_rcp_f32_e32 v221, v221
	v_mul_f32_e32 v240, v240, v217
	v_rcp_f32_e32 v222, v222
	v_mul_f32_e32 v241, v241, v218
	v_rcp_f32_e32 v223, v223
	v_mul_f32_e32 v242, v242, v219
	v_rcp_f32_e32 v224, v224
	v_mul_f32_e32 v243, v243, v220
	v_mfma_f32_32x32x16_bf16 v[18:33], v[58:61], v[150:153], v[18:33]
	v_exp_f32_e32 v246, v5
	v_fma_f32 v194, v221, v194, v240
	v_exp_f32_e32 v247, v9
	v_fma_f32 v195, v222, v195, v241
	v_exp_f32_e32 v248, v13
	v_fma_f32 v196, v223, v196, v242
	v_exp_f32_e32 v249, v17
	v_fma_f32 v197, v224, v197, v243
	v_mfma_f32_32x32x16_bf16 v[18:33], v[54:57], v[154:157], v[18:33]
	v_exp_f32_e32 v212, v194
	v_add_f32_e32 v246, 1.0, v246
	v_exp_f32_e32 v213, v195
	v_add_f32_e32 v247, 1.0, v247
	v_exp_f32_e32 v214, v196
	v_add_f32_e32 v248, 1.0, v248
	v_exp_f32_e32 v215, v197
	v_add_f32_e32 v249, 1.0, v249
	v_fmac_f32_e32 v246, v246, v212
	v_fmac_f32_e32 v247, v247, v213
	v_fmac_f32_e32 v248, v248, v214
	v_fmac_f32_e32 v249, v249, v215
	v_mfma_f32_32x32x16_bf16 v[18:33], v[50:53], v[158:161], v[18:33]
	v_rcp_f32_e32 v246, v246
	v_rcp_f32_e32 v247, v247
	v_rcp_f32_e32 v248, v248
	v_rcp_f32_e32 v249, v249
	v_fma_f32 v246, -v212, v246, v246
	v_fma_f32 v247, -v213, v247, v247
	v_fma_f32 v248, -v214, v248, v248
	v_fma_f32 v249, -v215, v249, v249
	v_cvt_pk_bf16_f32 v246, v246, v247
	v_cvt_pk_bf16_f32 v247, v248, v249
	ds_write_b64 v211, v[246:247] offset:0
	s_waitcnt lgkmcnt(1)
	v_mfma_f32_32x32x16_bf16 v[34:49], v[126:129], v[162:165], v[34:49]
	v_add_u32_e32 v233, v231, v244
	ds_read_b128 v[2:5], v233 offset:0
	ds_read_b128 v[6:9], v233 offset:16
	ds_read_b128 v[10:13], v233 offset:32
	ds_read_b128 v[14:17], v233 offset:48
	v_exp_f32_e32 v212, v20
	v_exp_f32_e32 v213, v24
	v_exp_f32_e32 v214, v28
	v_exp_f32_e32 v215, v32
	v_mfma_f32_32x32x16_bf16 v[34:49], v[122:125], v[166:169], v[34:49]
	v_exp_f32_e32 v217, v18
	v_add_f32_e32 v251, 1.0, v212
	v_exp_f32_e32 v218, v22
	v_add_f32_e32 v252, 1.0, v213
	v_exp_f32_e32 v219, v26
	v_add_f32_e32 v253, 1.0, v214
	v_exp_f32_e32 v220, v30
	v_add_f32_e32 v254, 1.0, v215
	v_fma_f32 v240, v212, s12, v235
	v_fma_f32 v241, v213, s12, v235
	v_fma_f32 v242, v214, s12, v235
	v_fma_f32 v243, v215, s12, v235
	v_mfma_f32_32x32x16_bf16 v[34:49], v[118:121], v[170:173], v[34:49]
	v_exp_f32_e32 v221, v19
	v_fmac_f32_e32 v251, v217, v251
	v_exp_f32_e32 v222, v23
	v_fmac_f32_e32 v252, v218, v252
	v_exp_f32_e32 v223, v27
	v_fmac_f32_e32 v253, v219, v253
	v_exp_f32_e32 v224, v31
	v_fmac_f32_e32 v254, v220, v254
	v_mfma_f32_32x32x16_bf16 v[34:49], v[114:117], v[174:177], v[34:49]
	v_rcp_f32_e32 v217, v251
	v_add_f32_e32 v221, 1.0, v221
	v_rcp_f32_e32 v218, v252
	v_add_f32_e32 v222, 1.0, v222
	v_rcp_f32_e32 v219, v253
	v_add_f32_e32 v223, 1.0, v223
	v_rcp_f32_e32 v220, v254
	v_add_f32_e32 v224, 1.0, v224
	v_mfma_f32_32x32x16_bf16 v[34:49], v[110:113], v[178:181], v[34:49]
	v_rcp_f32_e32 v221, v221
	v_mul_f32_e32 v240, v240, v217
	v_rcp_f32_e32 v222, v222
	v_mul_f32_e32 v241, v241, v218
	v_rcp_f32_e32 v223, v223
	v_mul_f32_e32 v242, v242, v219
	v_rcp_f32_e32 v224, v224
	v_mul_f32_e32 v243, v243, v220
	v_mfma_f32_32x32x16_bf16 v[34:49], v[106:109], v[182:185], v[34:49]
	v_exp_f32_e32 v246, v21
	v_fma_f32 v198, v221, v198, v240
	v_exp_f32_e32 v247, v25
	v_fma_f32 v199, v222, v199, v241
	v_exp_f32_e32 v248, v29
	v_fma_f32 v200, v223, v200, v242
	v_exp_f32_e32 v249, v33
	v_fma_f32 v201, v224, v201, v243
	v_mfma_f32_32x32x16_bf16 v[34:49], v[102:105], v[186:189], v[34:49]
	v_exp_f32_e32 v212, v198
	v_add_f32_e32 v246, 1.0, v246
	v_exp_f32_e32 v213, v199
	v_add_f32_e32 v247, 1.0, v247
	v_exp_f32_e32 v214, v200
	v_add_f32_e32 v248, 1.0, v248
	v_exp_f32_e32 v215, v201
	v_add_f32_e32 v249, 1.0, v249
	v_fmac_f32_e32 v246, v246, v212
	v_fmac_f32_e32 v247, v247, v213
	v_fmac_f32_e32 v248, v248, v214
	v_fmac_f32_e32 v249, v249, v215
	v_mfma_f32_32x32x16_bf16 v[34:49], v[98:101], v[190:193], v[34:49]
	v_rcp_f32_e32 v246, v246
	v_rcp_f32_e32 v247, v247
	v_rcp_f32_e32 v248, v248
	v_rcp_f32_e32 v249, v249
	v_fma_f32 v246, -v212, v246, v246
	v_fma_f32 v247, -v213, v247, v247
	v_fma_f32 v248, -v214, v248, v248
	v_fma_f32 v249, -v215, v249, v249
	v_cvt_pk_bf16_f32 v246, v246, v247
	v_cvt_pk_bf16_f32 v247, v248, v249
	ds_write_b64 v211, v[246:247] offset:8
	s_waitcnt lgkmcnt(0)
	s_barrier
	v_mfma_f32_32x32x16_bf16 v[82:97], v[78:81], v[162:165], v[82:97]
	ds_read_b128 v[130:133], v210 offset:0
	ds_read_b128 v[134:137], v210 offset:1024
	ds_read_b128 v[18:21], v233 offset:128
	ds_read_b128 v[22:25], v233 offset:144
	ds_read_b128 v[26:29], v233 offset:160
	ds_read_b128 v[30:33], v233 offset:176
	ds_read_b32 v245, v232 offset:128
	v_exp_f32_e32 v212, v36
	v_exp_f32_e32 v213, v40
	v_exp_f32_e32 v214, v44
	v_exp_f32_e32 v215, v48
	v_mfma_f32_32x32x16_bf16 v[82:97], v[74:77], v[166:169], v[82:97]
	ds_read_b128 v[138:141], v210 offset:2048
	ds_read_b128 v[142:145], v210 offset:3072
	v_exp_f32_e32 v217, v34
	v_add_f32_e32 v251, 1.0, v212
	v_exp_f32_e32 v218, v38
	v_add_f32_e32 v252, 1.0, v213
	v_exp_f32_e32 v219, v42
	v_add_f32_e32 v253, 1.0, v214
	v_exp_f32_e32 v220, v46
	v_add_f32_e32 v254, 1.0, v215
	v_fma_f32 v240, v212, s12, v235
	v_fma_f32 v241, v213, s12, v235
	v_fma_f32 v242, v214, s12, v235
	v_fma_f32 v243, v215, s12, v235
	v_mfma_f32_32x32x16_bf16 v[82:97], v[70:73], v[170:173], v[82:97]
	ds_read_b128 v[146:149], v210 offset:4096
	ds_read_b128 v[150:153], v210 offset:5120
	v_exp_f32_e32 v221, v35
	v_fmac_f32_e32 v251, v217, v251
	v_exp_f32_e32 v222, v39
	v_fmac_f32_e32 v252, v218, v252
	v_exp_f32_e32 v223, v43
	v_fmac_f32_e32 v253, v219, v253
	v_exp_f32_e32 v224, v47
	v_fmac_f32_e32 v254, v220, v254
	v_mfma_f32_32x32x16_bf16 v[82:97], v[66:69], v[174:177], v[82:97]
	ds_read_b128 v[154:157], v210 offset:6144
	ds_read_b128 v[158:161], v210 offset:7168
	v_rcp_f32_e32 v217, v251
	v_add_f32_e32 v221, 1.0, v221
	v_rcp_f32_e32 v218, v252
	v_add_f32_e32 v222, 1.0, v222
	v_rcp_f32_e32 v219, v253
	v_add_f32_e32 v223, 1.0, v223
	v_rcp_f32_e32 v220, v254
	v_add_f32_e32 v224, 1.0, v224
	v_mfma_f32_32x32x16_bf16 v[82:97], v[62:65], v[178:181], v[82:97]
	v_rcp_f32_e32 v221, v221
	v_mul_f32_e32 v240, v240, v217
	v_rcp_f32_e32 v222, v222
	v_mul_f32_e32 v241, v241, v218
	v_rcp_f32_e32 v223, v223
	v_mul_f32_e32 v242, v242, v219
	v_rcp_f32_e32 v224, v224
	v_mul_f32_e32 v243, v243, v220
	v_mfma_f32_32x32x16_bf16 v[82:97], v[58:61], v[182:185], v[82:97]
	v_exp_f32_e32 v246, v37
	v_fma_f32 v202, v221, v202, v240
	v_exp_f32_e32 v247, v41
	v_fma_f32 v203, v222, v203, v241
	v_exp_f32_e32 v248, v45
	v_fma_f32 v204, v223, v204, v242
	v_exp_f32_e32 v249, v49
	v_fma_f32 v205, v224, v205, v243
	v_mfma_f32_32x32x16_bf16 v[82:97], v[54:57], v[186:189], v[82:97]
	v_exp_f32_e32 v212, v202
	v_add_f32_e32 v246, 1.0, v246
	v_exp_f32_e32 v213, v203
	v_add_f32_e32 v247, 1.0, v247
	v_exp_f32_e32 v214, v204
	v_add_f32_e32 v248, 1.0, v248
	v_exp_f32_e32 v215, v205
	v_add_f32_e32 v249, 1.0, v249
	v_fmac_f32_e32 v246, v246, v212
	v_fmac_f32_e32 v247, v247, v213
	v_fmac_f32_e32 v248, v248, v214
	v_fmac_f32_e32 v249, v249, v215
	v_mfma_f32_32x32x16_bf16 v[82:97], v[50:53], v[190:193], v[82:97]
	v_rcp_f32_e32 v246, v246
	v_rcp_f32_e32 v247, v247
	v_rcp_f32_e32 v248, v248
	v_rcp_f32_e32 v249, v249
	v_fma_f32 v246, -v212, v246, v246
	v_fma_f32 v247, -v213, v247, v247
	v_fma_f32 v248, -v214, v248, v248
	v_fma_f32 v249, -v215, v249, v249
	v_cvt_pk_bf16_f32 v246, v246, v247
	v_cvt_pk_bf16_f32 v247, v248, v249
	ds_write_b64 v211, v[246:247] offset:8192
	s_waitcnt lgkmcnt(1)
	v_mfma_f32_32x32x16_bf16 v[2:17], v[126:129], v[130:133], v[2:17]
	v_add_u32_e32 v234, v231, v245
	ds_read_b128 v[34:37], v234 offset:0
	ds_read_b128 v[38:41], v234 offset:16
	ds_read_b128 v[42:45], v234 offset:32
	ds_read_b128 v[46:49], v234 offset:48
	v_add_u32_e32 v232, 0x100, v232
	v_exp_f32_e32 v212, v84
	v_exp_f32_e32 v213, v88
	v_exp_f32_e32 v214, v92
	v_exp_f32_e32 v215, v96
	v_mfma_f32_32x32x16_bf16 v[2:17], v[122:125], v[134:137], v[2:17]
	v_exp_f32_e32 v217, v82
	v_add_f32_e32 v251, 1.0, v212
	v_exp_f32_e32 v218, v86
	v_add_f32_e32 v252, 1.0, v213
	v_exp_f32_e32 v219, v90
	v_add_f32_e32 v253, 1.0, v214
	v_exp_f32_e32 v220, v94
	v_add_f32_e32 v254, 1.0, v215
	v_fma_f32 v240, v212, s12, v235
	v_fma_f32 v241, v213, s12, v235
	v_fma_f32 v242, v214, s12, v235
	v_fma_f32 v243, v215, s12, v235
	v_mfma_f32_32x32x16_bf16 v[2:17], v[118:121], v[138:141], v[2:17]
	v_exp_f32_e32 v221, v83
	v_fmac_f32_e32 v251, v217, v251
	v_exp_f32_e32 v222, v87
	v_fmac_f32_e32 v252, v218, v252
	v_exp_f32_e32 v223, v91
	v_fmac_f32_e32 v253, v219, v253
	v_exp_f32_e32 v224, v95
	v_fmac_f32_e32 v254, v220, v254
	v_mfma_f32_32x32x16_bf16 v[2:17], v[114:117], v[142:145], v[2:17]
	v_rcp_f32_e32 v217, v251
	v_add_f32_e32 v221, 1.0, v221
	v_rcp_f32_e32 v218, v252
	v_add_f32_e32 v222, 1.0, v222
	v_rcp_f32_e32 v219, v253
	v_add_f32_e32 v223, 1.0, v223
	v_rcp_f32_e32 v220, v254
	v_add_f32_e32 v224, 1.0, v224
	v_mfma_f32_32x32x16_bf16 v[2:17], v[110:113], v[146:149], v[2:17]
	v_rcp_f32_e32 v221, v221
	v_mul_f32_e32 v240, v240, v217
	v_rcp_f32_e32 v222, v222
	v_mul_f32_e32 v241, v241, v218
	v_rcp_f32_e32 v223, v223
	v_mul_f32_e32 v242, v242, v219
	v_rcp_f32_e32 v224, v224
	v_mul_f32_e32 v243, v243, v220
	v_mfma_f32_32x32x16_bf16 v[2:17], v[106:109], v[150:153], v[2:17]
	v_exp_f32_e32 v246, v85
	v_fma_f32 v206, v221, v206, v240
	v_exp_f32_e32 v247, v89
	v_fma_f32 v207, v222, v207, v241
	v_exp_f32_e32 v248, v93
	v_fma_f32 v208, v223, v208, v242
	v_exp_f32_e32 v249, v97
	v_fma_f32 v209, v224, v209, v243
	v_mfma_f32_32x32x16_bf16 v[2:17], v[102:105], v[154:157], v[2:17]
	v_exp_f32_e32 v212, v206
	v_add_f32_e32 v246, 1.0, v246
	v_exp_f32_e32 v213, v207
	v_add_f32_e32 v247, 1.0, v247
	v_exp_f32_e32 v214, v208
	v_add_f32_e32 v248, 1.0, v248
	v_exp_f32_e32 v215, v209
	v_add_f32_e32 v249, 1.0, v249
	v_fmac_f32_e32 v246, v246, v212
	v_fmac_f32_e32 v247, v247, v213
	v_fmac_f32_e32 v248, v248, v214
	v_fmac_f32_e32 v249, v249, v215
	v_mfma_f32_32x32x16_bf16 v[2:17], v[98:101], v[158:161], v[2:17]
	v_rcp_f32_e32 v246, v246
	v_rcp_f32_e32 v247, v247
	v_rcp_f32_e32 v248, v248
	v_rcp_f32_e32 v249, v249
	v_fma_f32 v246, -v212, v246, v246
	v_fma_f32 v247, -v213, v247, v247
	v_fma_f32 v248, -v214, v248, v248
	v_fma_f32 v249, -v215, v249, v249
	v_cvt_pk_bf16_f32 v246, v246, v247
	v_cvt_pk_bf16_f32 v247, v248, v249
	ds_write_b64 v211, v[246:247] offset:8200
	s_waitcnt lgkmcnt(0)
	s_barrier
	s_sub_u32 s16, s16, 1
	s_cmp_lg_u32 s16, 0
	s_cbranch_scc1 .Llight_loop
	v_mfma_f32_32x32x16_bf16 v[18:33], v[78:81], v[130:133], v[18:33]
	ds_read_b128 v[162:165], v210 offset:8192
	ds_read_b128 v[166:169], v210 offset:9216
	ds_read_b128 v[82:85], v234 offset:128
	ds_read_b128 v[86:89], v234 offset:144
	ds_read_b128 v[90:93], v234 offset:160
	ds_read_b128 v[94:97], v234 offset:176
	v_exp_f32_e32 v212, v4
	v_exp_f32_e32 v213, v8
	v_exp_f32_e32 v214, v12
	v_exp_f32_e32 v215, v16
	v_mfma_f32_32x32x16_bf16 v[18:33], v[74:77], v[134:137], v[18:33]
	ds_read_b128 v[170:173], v210 offset:10240
	ds_read_b128 v[174:177], v210 offset:11264
	v_exp_f32_e32 v217, v2
	v_add_f32_e32 v251, 1.0, v212
	v_exp_f32_e32 v218, v6
	v_add_f32_e32 v252, 1.0, v213
	v_exp_f32_e32 v219, v10
	v_add_f32_e32 v253, 1.0, v214
	v_exp_f32_e32 v220, v14
	v_add_f32_e32 v254, 1.0, v215
	v_fma_f32 v240, v212, s12, v235
	v_fma_f32 v241, v213, s12, v235
	v_fma_f32 v242, v214, s12, v235
	v_fma_f32 v243, v215, s12, v235
	v_mfma_f32_32x32x16_bf16 v[18:33], v[70:73], v[138:141], v[18:33]
	ds_read_b128 v[178:181], v210 offset:12288
	ds_read_b128 v[182:185], v210 offset:13312
	v_exp_f32_e32 v221, v3
	v_fmac_f32_e32 v251, v217, v251
	v_exp_f32_e32 v222, v7
	v_fmac_f32_e32 v252, v218, v252
	v_exp_f32_e32 v223, v11
	v_fmac_f32_e32 v253, v219, v253
	v_exp_f32_e32 v224, v15
	v_fmac_f32_e32 v254, v220, v254
	v_mfma_f32_32x32x16_bf16 v[18:33], v[66:69], v[142:145], v[18:33]
	ds_read_b128 v[186:189], v210 offset:14336
	ds_read_b128 v[190:193], v210 offset:15360
	v_rcp_f32_e32 v217, v251
	v_add_f32_e32 v221, 1.0, v221
	v_rcp_f32_e32 v218, v252
	v_add_f32_e32 v222, 1.0, v222
	v_rcp_f32_e32 v219, v253
	v_add_f32_e32 v223, 1.0, v223
	v_rcp_f32_e32 v220, v254
	v_add_f32_e32 v224, 1.0, v224
	v_mfma_f32_32x32x16_bf16 v[18:33], v[62:65], v[146:149], v[18:33]
	v_rcp_f32_e32 v221, v221
	v_mul_f32_e32 v240, v240, v217
	v_rcp_f32_e32 v222, v222
	v_mul_f32_e32 v241, v241, v218
	v_rcp_f32_e32 v223, v223
	v_mul_f32_e32 v242, v242, v219
	v_rcp_f32_e32 v224, v224
	v_mul_f32_e32 v243, v243, v220
	v_mfma_f32_32x32x16_bf16 v[18:33], v[58:61], v[150:153], v[18:33]
	v_exp_f32_e32 v246, v5
	v_fma_f32 v194, v221, v194, v240
	v_exp_f32_e32 v247, v9
	v_fma_f32 v195, v222, v195, v241
	v_exp_f32_e32 v248, v13
	v_fma_f32 v196, v223, v196, v242
	v_exp_f32_e32 v249, v17
	v_fma_f32 v197, v224, v197, v243
	v_mfma_f32_32x32x16_bf16 v[18:33], v[54:57], v[154:157], v[18:33]
	v_exp_f32_e32 v212, v194
	v_add_f32_e32 v246, 1.0, v246
	v_exp_f32_e32 v213, v195
	v_add_f32_e32 v247, 1.0, v247
	v_exp_f32_e32 v214, v196
	v_add_f32_e32 v248, 1.0, v248
	v_exp_f32_e32 v215, v197
	v_add_f32_e32 v249, 1.0, v249
	v_fmac_f32_e32 v246, v246, v212
	v_fmac_f32_e32 v247, v247, v213
	v_fmac_f32_e32 v248, v248, v214
	v_fmac_f32_e32 v249, v249, v215
	v_mfma_f32_32x32x16_bf16 v[18:33], v[50:53], v[158:161], v[18:33]
	v_rcp_f32_e32 v246, v246
	v_rcp_f32_e32 v247, v247
	v_rcp_f32_e32 v248, v248
	v_rcp_f32_e32 v249, v249
	v_fma_f32 v246, -v212, v246, v246
	v_fma_f32 v247, -v213, v247, v247
	v_fma_f32 v248, -v214, v248, v248
	v_fma_f32 v249, -v215, v249, v249
	v_cvt_pk_bf16_f32 v246, v246, v247
	v_cvt_pk_bf16_f32 v247, v248, v249
	ds_write_b64 v211, v[246:247] offset:0
	s_waitcnt lgkmcnt(1)
	v_mfma_f32_32x32x16_bf16 v[34:49], v[126:129], v[162:165], v[34:49]
	v_exp_f32_e32 v212, v20
	v_exp_f32_e32 v213, v24
	v_exp_f32_e32 v214, v28
	v_exp_f32_e32 v215, v32
	v_mfma_f32_32x32x16_bf16 v[34:49], v[122:125], v[166:169], v[34:49]
	v_exp_f32_e32 v217, v18
	v_add_f32_e32 v251, 1.0, v212
	v_exp_f32_e32 v218, v22
	v_add_f32_e32 v252, 1.0, v213
	v_exp_f32_e32 v219, v26
	v_add_f32_e32 v253, 1.0, v214
	v_exp_f32_e32 v220, v30
	v_add_f32_e32 v254, 1.0, v215
	v_fma_f32 v240, v212, s12, v235
	v_fma_f32 v241, v213, s12, v235
	v_fma_f32 v242, v214, s12, v235
	v_fma_f32 v243, v215, s12, v235
	v_mfma_f32_32x32x16_bf16 v[34:49], v[118:121], v[170:173], v[34:49]
	v_exp_f32_e32 v221, v19
	v_fmac_f32_e32 v251, v217, v251
	v_exp_f32_e32 v222, v23
	v_fmac_f32_e32 v252, v218, v252
	v_exp_f32_e32 v223, v27
	v_fmac_f32_e32 v253, v219, v253
	v_exp_f32_e32 v224, v31
	v_fmac_f32_e32 v254, v220, v254
	v_mfma_f32_32x32x16_bf16 v[34:49], v[114:117], v[174:177], v[34:49]
	v_rcp_f32_e32 v217, v251
	v_add_f32_e32 v221, 1.0, v221
	v_rcp_f32_e32 v218, v252
	v_add_f32_e32 v222, 1.0, v222
	v_rcp_f32_e32 v219, v253
	v_add_f32_e32 v223, 1.0, v223
	v_rcp_f32_e32 v220, v254
	v_add_f32_e32 v224, 1.0, v224
	v_mfma_f32_32x32x16_bf16 v[34:49], v[110:113], v[178:181], v[34:49]
	v_rcp_f32_e32 v221, v221
	v_mul_f32_e32 v240, v240, v217
	v_rcp_f32_e32 v222, v222
	v_mul_f32_e32 v241, v241, v218
	v_rcp_f32_e32 v223, v223
	v_mul_f32_e32 v242, v242, v219
	v_rcp_f32_e32 v224, v224
	v_mul_f32_e32 v243, v243, v220
	v_mfma_f32_32x32x16_bf16 v[34:49], v[106:109], v[182:185], v[34:49]
	v_exp_f32_e32 v246, v21
	v_fma_f32 v198, v221, v198, v240
	v_exp_f32_e32 v247, v25
	v_fma_f32 v199, v222, v199, v241
	v_exp_f32_e32 v248, v29
	v_fma_f32 v200, v223, v200, v242
	v_exp_f32_e32 v249, v33
	v_fma_f32 v201, v224, v201, v243
	v_mfma_f32_32x32x16_bf16 v[34:49], v[102:105], v[186:189], v[34:49]
	v_exp_f32_e32 v212, v198
	v_add_f32_e32 v246, 1.0, v246
	v_exp_f32_e32 v213, v199
	v_add_f32_e32 v247, 1.0, v247
	v_exp_f32_e32 v214, v200
	v_add_f32_e32 v248, 1.0, v248
	v_exp_f32_e32 v215, v201
	v_add_f32_e32 v249, 1.0, v249
	v_fmac_f32_e32 v246, v246, v212
	v_fmac_f32_e32 v247, v247, v213
	v_fmac_f32_e32 v248, v248, v214
	v_fmac_f32_e32 v249, v249, v215
	v_mfma_f32_32x32x16_bf16 v[34:49], v[98:101], v[190:193], v[34:49]
	v_rcp_f32_e32 v246, v246
	v_rcp_f32_e32 v247, v247
	v_rcp_f32_e32 v248, v248
	v_rcp_f32_e32 v249, v249
	v_fma_f32 v246, -v212, v246, v246
	v_fma_f32 v247, -v213, v247, v247
	v_fma_f32 v248, -v214, v248, v248
	v_fma_f32 v249, -v215, v249, v249
	v_cvt_pk_bf16_f32 v246, v246, v247
	v_cvt_pk_bf16_f32 v247, v248, v249
	ds_write_b64 v211, v[246:247] offset:8
	s_waitcnt lgkmcnt(0)
	s_barrier
	s_bfe_u32 s20, s19, 0x10006
	s_lshl_b32 s21, s20, 7
	s_lshl_b32 s20, s20, 13
	s_add_u32 s20, s20, 0x30000
	s_add_u32 s22, s14, s20
	s_addc_u32 s23, s15, 0
	s_add_u32 s24, s22, 0x1000
	s_addc_u32 s25, s23, 0
	global_load_dwordx4 v[130:133], v210, s[22:23] offset:0
	global_load_dwordx4 v[130:133], v210, s[22:23] offset:1024
	global_load_dwordx4 v[130:133], v210, s[22:23] offset:2048
	global_load_dwordx4 v[130:133], v210, s[22:23] offset:3072
	global_load_dwordx4 v[130:133], v210, s[24:25] offset:0
	global_load_dwordx4 v[130:133], v210, s[24:25] offset:1024
	global_load_dwordx4 v[130:133], v210, s[24:25] offset:2048
	global_load_dwordx4 v[130:133], v210, s[24:25] offset:3072
	v_or_b32_e32 v138, s21, v230
	global_load_dwordx4 v[134:137], v138, s[4:5] offset:0
	global_load_dwordx4 v[134:137], v138, s[4:5] offset:32
	global_load_dwordx4 v[134:137], v138, s[4:5] offset:64
	global_load_dwordx4 v[134:137], v138, s[4:5] offset:96
	global_load_dwordx4 v[134:137], v138, s[6:7] offset:0
	global_load_dwordx4 v[134:137], v138, s[6:7] offset:32
	global_load_dwordx4 v[134:137], v138, s[6:7] offset:64
	global_load_dwordx4 v[134:137], v138, s[6:7] offset:96
	s_load_dword s21, s[8:9], 0x0
	v_mfma_f32_32x32x16_bf16 v[82:97], v[78:81], v[162:165], v[82:97]
	v_exp_f32_e32 v212, v36
	v_exp_f32_e32 v213, v40
	v_exp_f32_e32 v214, v44
	v_exp_f32_e32 v215, v48
	v_mfma_f32_32x32x16_bf16 v[82:97], v[74:77], v[166:169], v[82:97]
	v_exp_f32_e32 v217, v34
	v_add_f32_e32 v251, 1.0, v212
	v_exp_f32_e32 v218, v38
	v_add_f32_e32 v252, 1.0, v213
	v_exp_f32_e32 v219, v42
	v_add_f32_e32 v253, 1.0, v214
	v_exp_f32_e32 v220, v46
	v_add_f32_e32 v254, 1.0, v215
	v_fma_f32 v240, v212, s12, v235
	v_fma_f32 v241, v213, s12, v235
	v_fma_f32 v242, v214, s12, v235
	v_fma_f32 v243, v215, s12, v235
	v_mfma_f32_32x32x16_bf16 v[82:97], v[70:73], v[170:173], v[82:97]
	v_exp_f32_e32 v221, v35
	v_fmac_f32_e32 v251, v217, v251
	v_exp_f32_e32 v222, v39
	v_fmac_f32_e32 v252, v218, v252
	v_exp_f32_e32 v223, v43
	v_fmac_f32_e32 v253, v219, v253
	v_exp_f32_e32 v224, v47
	v_fmac_f32_e32 v254, v220, v254
	v_mfma_f32_32x32x16_bf16 v[82:97], v[66:69], v[174:177], v[82:97]
	v_rcp_f32_e32 v217, v251
	v_add_f32_e32 v221, 1.0, v221
	v_rcp_f32_e32 v218, v252
	v_add_f32_e32 v222, 1.0, v222
	v_rcp_f32_e32 v219, v253
	v_add_f32_e32 v223, 1.0, v223
	v_rcp_f32_e32 v220, v254
	v_add_f32_e32 v224, 1.0, v224
	v_mfma_f32_32x32x16_bf16 v[82:97], v[62:65], v[178:181], v[82:97]
	v_rcp_f32_e32 v221, v221
	v_mul_f32_e32 v240, v240, v217
	v_rcp_f32_e32 v222, v222
	v_mul_f32_e32 v241, v241, v218
	v_rcp_f32_e32 v223, v223
	v_mul_f32_e32 v242, v242, v219
	v_rcp_f32_e32 v224, v224
	v_mul_f32_e32 v243, v243, v220
	v_mfma_f32_32x32x16_bf16 v[82:97], v[58:61], v[182:185], v[82:97]
	v_exp_f32_e32 v246, v37
	v_fma_f32 v202, v221, v202, v240
	v_exp_f32_e32 v247, v41
	v_fma_f32 v203, v222, v203, v241
	v_exp_f32_e32 v248, v45
	v_fma_f32 v204, v223, v204, v242
	v_exp_f32_e32 v249, v49
	v_fma_f32 v205, v224, v205, v243
	v_mfma_f32_32x32x16_bf16 v[82:97], v[54:57], v[186:189], v[82:97]
	v_exp_f32_e32 v212, v202
	v_add_f32_e32 v246, 1.0, v246
	v_exp_f32_e32 v213, v203
	v_add_f32_e32 v247, 1.0, v247
	v_exp_f32_e32 v214, v204
	v_add_f32_e32 v248, 1.0, v248
	v_exp_f32_e32 v215, v205
	v_add_f32_e32 v249, 1.0, v249
	v_fmac_f32_e32 v246, v246, v212
	v_fmac_f32_e32 v247, v247, v213
	v_fmac_f32_e32 v248, v248, v214
	v_fmac_f32_e32 v249, v249, v215
	v_mfma_f32_32x32x16_bf16 v[82:97], v[50:53], v[190:193], v[82:97]
	v_rcp_f32_e32 v246, v246
	v_rcp_f32_e32 v247, v247
	v_rcp_f32_e32 v248, v248
	v_rcp_f32_e32 v249, v249
	v_fma_f32 v246, -v212, v246, v246
	v_fma_f32 v247, -v213, v247, v247
	v_fma_f32 v248, -v214, v248, v248
	v_fma_f32 v249, -v215, v249, v249
	v_cvt_pk_bf16_f32 v246, v246, v247
	v_cvt_pk_bf16_f32 v247, v248, v249
	ds_write_b64 v211, v[246:247] offset:8192
	s_waitcnt lgkmcnt(1)
	v_exp_f32_e32 v212, v84
	v_exp_f32_e32 v213, v88
	v_exp_f32_e32 v214, v92
	v_exp_f32_e32 v215, v96
	v_exp_f32_e32 v217, v82
	v_add_f32_e32 v251, 1.0, v212
	v_exp_f32_e32 v218, v86
	v_add_f32_e32 v252, 1.0, v213
	v_exp_f32_e32 v219, v90
	v_add_f32_e32 v253, 1.0, v214
	v_exp_f32_e32 v220, v94
	v_add_f32_e32 v254, 1.0, v215
	v_fma_f32 v240, v212, s12, v235
	v_fma_f32 v241, v213, s12, v235
	v_fma_f32 v242, v214, s12, v235
	v_fma_f32 v243, v215, s12, v235
	v_exp_f32_e32 v221, v83
	v_fmac_f32_e32 v251, v217, v251
	v_exp_f32_e32 v222, v87
	v_fmac_f32_e32 v252, v218, v252
	v_exp_f32_e32 v223, v91
	v_fmac_f32_e32 v253, v219, v253
	v_exp_f32_e32 v224, v95
	v_fmac_f32_e32 v254, v220, v254
	v_rcp_f32_e32 v217, v251
	v_add_f32_e32 v221, 1.0, v221
	v_rcp_f32_e32 v218, v252
	v_add_f32_e32 v222, 1.0, v222
	v_rcp_f32_e32 v219, v253
	v_add_f32_e32 v223, 1.0, v223
	v_rcp_f32_e32 v220, v254
	v_add_f32_e32 v224, 1.0, v224
	v_rcp_f32_e32 v221, v221
	v_mul_f32_e32 v240, v240, v217
	v_rcp_f32_e32 v222, v222
	v_mul_f32_e32 v241, v241, v218
	v_rcp_f32_e32 v223, v223
	v_mul_f32_e32 v242, v242, v219
	v_rcp_f32_e32 v224, v224
	v_mul_f32_e32 v243, v243, v220
	v_exp_f32_e32 v246, v85
	v_fma_f32 v206, v221, v206, v240
	v_exp_f32_e32 v247, v89
	v_fma_f32 v207, v222, v207, v241
	v_exp_f32_e32 v248, v93
	v_fma_f32 v208, v223, v208, v242
	v_exp_f32_e32 v249, v97
	v_fma_f32 v209, v224, v209, v243
	v_exp_f32_e32 v212, v206
	v_add_f32_e32 v246, 1.0, v246
	v_exp_f32_e32 v213, v207
	v_add_f32_e32 v247, 1.0, v247
	v_exp_f32_e32 v214, v208
	v_add_f32_e32 v248, 1.0, v248
	v_exp_f32_e32 v215, v209
	v_add_f32_e32 v249, 1.0, v249
	v_fmac_f32_e32 v246, v246, v212
	v_fmac_f32_e32 v247, v247, v213
	v_fmac_f32_e32 v248, v248, v214
	v_fmac_f32_e32 v249, v249, v215
	v_rcp_f32_e32 v246, v246
	v_rcp_f32_e32 v247, v247
	v_rcp_f32_e32 v248, v248
	v_rcp_f32_e32 v249, v249
	v_fma_f32 v246, -v212, v246, v246
	v_fma_f32 v247, -v213, v247, v247
	v_fma_f32 v248, -v214, v248, v248
	v_fma_f32 v249, -v215, v249, v249
	v_cvt_pk_bf16_f32 v246, v246, v247
	v_cvt_pk_bf16_f32 v247, v248, v249
	ds_write_b64 v211, v[246:247] offset:8200
	s_waitcnt lgkmcnt(0)
	s_barrier
	s_waitcnt vmcnt(0)
	s_nop 7
	s_nop 7
	s_branch .Lepilogue
